# epilogue: K-half exchange adds moved before the grid-barrier wait; pre-loop block and topic loop regenerated on the exchanged-tile register layout
# speedup vs baseline: 1.0032x; 1.0032x over previous
.LBB1_21:
	s_or_b64 exec, exec, s[0:1]
	v_lshlrev_b32_e32 v73, 16, v225
	v_lshlrev_b32_e32 v84, 14, v224
	v_or3_b32 v66, v73, v213, v84
	v_lshlrev_b32_e32 v210, 2, v0
	v_mov_b32_e32 v211, 0
	ds_write_b128 v66, v[2:5]
	ds_write_b128 v66, v[6:9] offset:1024
	ds_write_b128 v66, v[10:13] offset:2048
	ds_write_b128 v66, v[14:17] offset:3072
	ds_write_b128 v66, v[34:37] offset:4096
	ds_write_b128 v66, v[38:41] offset:5120
	ds_write_b128 v66, v[42:45] offset:6144
	ds_write_b128 v66, v[46:49] offset:7168
	ds_write_b128 v66, v[50:53] offset:8192
	ds_write_b128 v66, v[54:57] offset:9216
	ds_write_b128 v66, v[58:61] offset:10240
	ds_write_b128 v66, v[62:65] offset:11264
	ds_write_b128 v66, v[18:21] offset:12288
	ds_write_b128 v66, v[22:25] offset:13312
	ds_write_b128 v66, v[26:29] offset:14336
	ds_write_b128 v66, v[30:33] offset:15360
	v_lshl_add_u64 v[66:67], s[18:19], 0, v[210:211]
	s_movk_i32 s0, 0x1000
	v_add_co_u32_e32 v68, vcc, s0, v66
	s_movk_i32 s0, 0x2000
	s_nop 0
	v_addc_co_u32_e32 v69, vcc, 0, v67, vcc
	v_add_co_u32_e32 v66, vcc, s0, v66
	s_waitcnt lgkmcnt(0)
	s_barrier
	global_load_dword v239, v210, s[18:19]
	global_load_dword v240, v210, s[18:19] offset:2048
	v_addc_co_u32_e32 v67, vcc, 0, v67, vcc
	global_load_dword v241, v[68:69], off offset:2048
	global_load_dword v242, v[66:67], off offset:-4096
	global_load_dword v243, v[66:67], off
	v_min_u32_e32 v66, 19, v212
	v_add_u32_e32 v66, s3, v66
	v_and_b32_e32 v238, 0x7f, v0
	v_ashrrev_i32_e32 v67, 31, v66
	v_lshlrev_b32_e32 v226, 2, v238
	v_lshl_add_u64 v[66:67], v[66:67], 2, s[22:23]
	global_load_dword v237, v226, s[30:31]
	global_load_dword v234, v226, s[12:13]
	global_load_dword v235, v226, s[28:29]
	global_load_dword v85, v[66:67], off
	v_cmp_gt_u32_e64 s[0:1], 20, v0
	v_lshrrev_b32_e32 v227, 7, v0
	v_lshrrev_b32_e32 v236, 5, v0
	v_cndmask_b32_e64 v66, 19, v0, s[0:1]
	v_lshlrev_b32_e32 v66, 2, v66
	global_load_dword v233, v66, s[26:27]
	v_mad_u32_u24 v66, v227, 5, s3
	v_lshl_or_b32 v66, v66, 7, v238
	v_add_u32_e32 v68, 0x80, v66
	v_ashrrev_i32_e32 v69, 31, v68
	v_lshl_add_u64 v[76:77], v[68:69], 2, s[16:17]
	v_add_u32_e32 v68, 0x100, v66
	v_ashrrev_i32_e32 v67, 31, v66
	v_ashrrev_i32_e32 v69, 31, v68
	v_lshl_add_u64 v[74:75], v[66:67], 2, s[16:17]
	v_lshl_add_u64 v[78:79], v[68:69], 2, s[16:17]
	v_add_u32_e32 v68, 0x180, v66
	v_add_u32_e32 v66, 0x200, v66
	v_ashrrev_i32_e32 v67, 31, v66
	v_ashrrev_i32_e32 v69, 31, v68
	v_lshl_add_u64 v[66:67], v[66:67], 2, s[16:17]
	v_lshl_add_u64 v[80:81], v[68:69], 2, s[16:17]
	global_load_dword v68, v[74:75], off
	global_load_dword v69, v[76:77], off
	global_load_dword v70, v[78:79], off
	global_load_dword v71, v[80:81], off
	global_load_dword v72, v[66:67], off
	v_lshlrev_b32_e32 v66, 4, v214
	v_mov_b32_e32 v67, v211
	v_lshl_add_u64 v[74:75], s[36:37], 0, v[66:67]
	v_lshlrev_b32_e32 v76, 12, v236
	v_mov_b32_e32 v77, v211
	v_lshl_add_u64 v[66:67], s[34:35], 0, v[66:67]
	v_lshl_add_u64 v[74:75], v[74:75], 0, v[76:77]
	v_lshl_add_u64 v[66:67], v[66:67], 0, v[76:77]
	global_load_dwordx4 v[206:209], v[74:75], off
	global_load_dwordx4 v[198:201], v[74:75], off offset:512
	global_load_dwordx4 v[202:205], v[66:67], off
	global_load_dwordx4 v[194:197], v[66:67], off offset:512
	global_load_dwordx4 v[190:193], v[74:75], off offset:1024
	global_load_dwordx4 v[182:185], v[74:75], off offset:1536
	global_load_dwordx4 v[186:189], v[66:67], off offset:1024
	global_load_dwordx4 v[178:181], v[66:67], off offset:1536
	global_load_dwordx4 v[174:177], v[74:75], off offset:2048
	global_load_dwordx4 v[166:169], v[74:75], off offset:2560
	global_load_dwordx4 v[170:173], v[66:67], off offset:2048
	global_load_dwordx4 v[162:165], v[66:67], off offset:2560
	global_load_dwordx4 v[158:161], v[74:75], off offset:3072
	global_load_dwordx4 v[150:153], v[74:75], off offset:3584
	global_load_dwordx4 v[154:157], v[66:67], off offset:3072
	global_load_dwordx4 v[146:149], v[66:67], off offset:3584
	v_mov_b32_e32 v66, 0xc8
	v_cmp_gt_u32_e32 vcc, 20, v212
	v_xor_b32_e32 v73, 0x10000, v73
	v_or3_b32 v73, v73, v213, v84
	ds_read_b128 v[142:145], v73
	ds_read_b128 v[138:141], v73 offset:1024
	ds_read_b128 v[134:137], v73 offset:2048
	ds_read_b128 v[130:133], v73 offset:3072
	ds_read_b128 v[126:129], v73 offset:4096
	ds_read_b128 v[122:125], v73 offset:5120
	ds_read_b128 v[118:121], v73 offset:6144
	ds_read_b128 v[114:117], v73 offset:7168
	ds_read_b128 v[110:113], v73 offset:8192
	ds_read_b128 v[106:109], v73 offset:9216
	ds_read_b128 v[98:101], v73 offset:10240
	ds_read_b128 v[90:93], v73 offset:11264
	s_waitcnt vmcnt(22)
	v_med3_i32 v66, v85, 0, v66
	v_cndmask_b32_e32 v66, 0, v66, vcc
	ds_bpermute_b32 v67, v232, v66
	s_waitcnt lgkmcnt(0)
	v_add_u32_e32 v66, v67, v66
	ds_bpermute_b32 v67, v231, v66
	s_waitcnt lgkmcnt(0)
	v_add_u32_e32 v66, v66, v67
	ds_bpermute_b32 v67, v230, v66
	s_waitcnt lgkmcnt(0)
	v_add_u32_e32 v66, v66, v67
	ds_bpermute_b32 v67, v229, v66
	s_waitcnt lgkmcnt(0)
	v_add_u32_e32 v66, v66, v67
	ds_bpermute_b32 v67, v228, v66
	s_waitcnt lgkmcnt(0)
	v_add_u32_e32 v66, v66, v67
	v_xor_b32_e32 v67, 32, v82
	v_cmp_lt_i32_e32 vcc, v67, v83
	s_nop 1
	v_cndmask_b32_e32 v67, v82, v67, vcc
	v_lshlrev_b32_e32 v67, 2, v67
	ds_bpermute_b32 v67, v67, v66
	ds_read_b128 v[102:105], v73 offset:12288
	ds_read_b128 v[94:97], v73 offset:13312
	ds_read_b128 v[86:89], v73 offset:14336
	ds_read_b128 v[82:85], v73 offset:15360
	s_load_dword s18, s[8:9], 0x0
	v_cmp_gt_u32_e32 vcc, 64, v0
	s_waitcnt lgkmcnt(0)
	v_add_f32_e32 v142, v142, v2
	v_add_f32_e32 v143, v143, v3
	v_add_f32_e32 v144, v144, v4
	v_add_f32_e32 v145, v145, v5
	v_add_f32_e32 v138, v138, v6
	v_add_f32_e32 v139, v139, v7
	v_add_f32_e32 v140, v140, v8
	v_add_f32_e32 v141, v141, v9
	v_add_f32_e32 v134, v134, v10
	v_add_f32_e32 v135, v135, v11
	v_add_f32_e32 v136, v136, v12
	v_add_f32_e32 v137, v137, v13
	v_add_f32_e32 v130, v130, v14
	v_add_f32_e32 v131, v131, v15
	v_add_f32_e32 v132, v132, v16
	v_add_f32_e32 v133, v133, v17
	v_add_f32_e32 v126, v126, v34
	v_add_f32_e32 v127, v127, v35
	v_add_f32_e32 v128, v128, v36
	v_add_f32_e32 v129, v129, v37
	v_add_f32_e32 v122, v122, v38
	v_add_f32_e32 v123, v123, v39
	v_add_f32_e32 v124, v124, v40
	v_add_f32_e32 v125, v125, v41
	v_add_f32_e32 v118, v118, v42
	v_add_f32_e32 v119, v119, v43
	v_add_f32_e32 v120, v120, v44
	v_add_f32_e32 v121, v121, v45
	v_add_f32_e32 v114, v114, v46
	v_add_f32_e32 v115, v115, v47
	v_add_f32_e32 v116, v116, v48
	v_add_f32_e32 v117, v117, v49
	v_add_f32_e32 v110, v110, v50
	v_add_f32_e32 v111, v111, v51
	v_add_f32_e32 v112, v112, v52
	v_add_f32_e32 v113, v113, v53
	v_add_f32_e32 v106, v106, v54
	v_add_f32_e32 v107, v107, v55
	v_add_f32_e32 v108, v108, v56
	v_add_f32_e32 v109, v109, v57
	v_add_f32_e32 v98, v98, v58
	v_add_f32_e32 v99, v99, v59
	v_add_f32_e32 v100, v100, v60
	v_add_f32_e32 v101, v101, v61
	v_add_f32_e32 v90, v90, v62
	v_add_f32_e32 v91, v91, v63
	v_add_f32_e32 v92, v92, v64
	v_add_f32_e32 v93, v93, v65
	v_add_f32_e32 v102, v102, v18
	v_add_f32_e32 v103, v103, v19
	v_add_f32_e32 v104, v104, v20
	v_add_f32_e32 v105, v105, v21
	v_add_f32_e32 v94, v94, v22
	v_add_f32_e32 v95, v95, v23
	v_add_f32_e32 v96, v96, v24
	v_add_f32_e32 v97, v97, v25
	v_add_f32_e32 v86, v86, v26
	v_add_f32_e32 v87, v87, v27
	v_add_f32_e32 v88, v88, v28
	v_add_f32_e32 v89, v89, v29
	v_add_f32_e32 v82, v82, v30
	v_add_f32_e32 v83, v83, v31
	v_add_f32_e32 v84, v84, v32
	v_add_f32_e32 v85, v85, v33
	v_add_u32_e32 v66, v66, v67
	v_cvt_f32_i32_e32 v73, v66
	s_barrier
	s_and_saveexec_b64 s[8:9], vcc
	s_cbranch_execz .LBB1_40
	v_lshlrev_b32_e32 v66, 8, v0
	v_mov_b32_e32 v67, v211
	v_cmp_gt_u32_e64 s[2:3], 8, v212
	v_lshl_add_u64 v[66:67], s[6:7], 0, v[66:67]
	s_mov_b32 s19, -5
	s_branch .LBB1_24

.LBB1_53:
	s_or_b64 exec, exec, s[2:3]
	v_or_b32_e32 v163, v212, v214
	v_add_u32_e32 v163, 0x17080, v163
	ds_read_b128 v[2:5], v163
	ds_read_b128 v[6:9], v163 offset:32
	ds_read_b128 v[10:13], v163 offset:64
	ds_read_b128 v[14:17], v163 offset:96
	v_mul_u32_u24_e32 v165, 10, v225
	v_lshlrev_b32_e32 v1, 9, v1
	v_lshlrev_b32_e32 v164, 9, v165
	v_lshl_or_b32 v1, v165, 12, v1
	v_lshlrev_b32_e32 v165, 10, v224
	v_or3_b32 v1, v165, v1, v211
	v_or3_b32 v164, v164, v212, v214
	v_add_u32_e32 v1, 0x2800, v1
	s_waitcnt lgkmcnt(0)
	v_add_f32_e32 v142, v2, v142
	v_add_f32_e32 v143, v3, v143
	v_add_f32_e32 v144, v4, v144
	v_add_f32_e32 v145, v5, v145
	v_add_f32_e32 v138, v6, v138
	v_add_f32_e32 v139, v7, v139
	v_add_f32_e32 v140, v8, v140
	v_add_f32_e32 v141, v9, v141
	v_add_f32_e32 v134, v10, v134
	v_add_f32_e32 v135, v11, v135
	v_add_f32_e32 v136, v12, v136
	v_add_f32_e32 v137, v13, v137
	v_add_f32_e32 v130, v14, v130
	v_add_f32_e32 v131, v15, v131
	v_add_f32_e32 v132, v16, v132
	v_add_f32_e32 v133, v17, v133
	v_add_f32_e32 v126, v2, v126
	v_add_f32_e32 v127, v3, v127
	v_add_f32_e32 v128, v4, v128
	v_add_f32_e32 v129, v5, v129
	v_add_f32_e32 v122, v6, v122
	v_add_f32_e32 v123, v7, v123
	v_add_f32_e32 v124, v8, v124
	v_add_f32_e32 v125, v9, v125
	v_add_f32_e32 v118, v10, v118
	v_add_f32_e32 v119, v11, v119
	v_add_f32_e32 v120, v12, v120
	v_add_f32_e32 v121, v13, v121
	v_add_f32_e32 v114, v14, v114
	v_add_f32_e32 v115, v15, v115
	v_add_f32_e32 v116, v16, v116
	v_add_f32_e32 v117, v17, v117
	v_add_f32_e32 v110, v2, v110
	v_add_f32_e32 v111, v3, v111
	v_add_f32_e32 v112, v4, v112
	v_add_f32_e32 v113, v5, v113
	v_add_f32_e32 v106, v6, v106
	v_add_f32_e32 v107, v7, v107
	v_add_f32_e32 v108, v8, v108
	v_add_f32_e32 v109, v9, v109
	v_add_f32_e32 v98, v10, v98
	v_add_f32_e32 v99, v11, v99
	v_add_f32_e32 v100, v12, v100
	v_add_f32_e32 v101, v13, v101
	v_add_f32_e32 v90, v14, v90
	v_add_f32_e32 v91, v15, v91
	v_add_f32_e32 v92, v16, v92
	v_add_f32_e32 v93, v17, v93
	v_add_f32_e32 v102, v2, v102
	v_add_f32_e32 v103, v3, v103
	v_add_f32_e32 v104, v4, v104
	v_add_f32_e32 v105, v5, v105
	v_add_f32_e32 v94, v6, v94
	v_add_f32_e32 v95, v7, v95
	v_add_f32_e32 v96, v8, v96
	v_add_f32_e32 v97, v9, v97
	v_add_f32_e32 v86, v10, v86
	v_add_f32_e32 v87, v11, v87
	v_add_f32_e32 v88, v12, v88
	v_add_f32_e32 v89, v13, v89
	v_add_f32_e32 v82, v14, v82
	v_add_f32_e32 v83, v15, v83
	v_add_f32_e32 v84, v16, v84
	v_add_f32_e32 v85, v17, v85
	s_waitcnt vmcnt(0)
	v_mul_f32_e32 v66, 0.5, v66
	v_mul_f32_e32 v67, 0.5, v67
	v_mul_f32_e32 v68, 0.5, v68
	v_mul_f32_e32 v69, 0.5, v69
	v_mul_f32_e32 v70, 0.5, v70
	v_mul_f32_e32 v71, 0.5, v71
	v_mul_f32_e32 v72, 0.5, v72
	v_mul_f32_e32 v73, 0.5, v73
	v_mul_f32_e32 v74, 0.5, v74
	v_mul_f32_e32 v75, 0.5, v75
	v_mul_f32_e32 v76, 0.5, v76
	v_mul_f32_e32 v77, 0.5, v77
	v_mul_f32_e32 v78, 0.5, v78
	v_mul_f32_e32 v79, 0.5, v79
	v_mul_f32_e32 v80, 0.5, v80
	v_mul_f32_e32 v81, 0.5, v81
	v_mul_f32_e32 v154, v66, v142
	v_mul_f32_e32 v155, v66, v126
	v_mul_f32_e32 v156, v66, v110
	v_mul_f32_e32 v157, v66, v102
	v_fmac_f32_e32 v154, v67, v143
	v_fmac_f32_e32 v155, v67, v127
	v_fmac_f32_e32 v156, v67, v111
	v_fmac_f32_e32 v157, v67, v103
	v_fmac_f32_e32 v154, v68, v144
	v_fmac_f32_e32 v155, v68, v128
	v_fmac_f32_e32 v156, v68, v112
	v_fmac_f32_e32 v157, v68, v104
	v_fmac_f32_e32 v154, v69, v145
	v_fmac_f32_e32 v155, v69, v129
	v_fmac_f32_e32 v156, v69, v113
	v_fmac_f32_e32 v157, v69, v105
	v_fmac_f32_e32 v154, v70, v138
	v_fmac_f32_e32 v155, v70, v122
	v_fmac_f32_e32 v156, v70, v106
	v_fmac_f32_e32 v157, v70, v94
	v_fmac_f32_e32 v154, v71, v139
	v_fmac_f32_e32 v155, v71, v123
	v_fmac_f32_e32 v156, v71, v107
	v_fmac_f32_e32 v157, v71, v95
	v_fmac_f32_e32 v154, v72, v140
	v_fmac_f32_e32 v155, v72, v124
	v_fmac_f32_e32 v156, v72, v108
	v_fmac_f32_e32 v157, v72, v96
	v_fmac_f32_e32 v154, v73, v141
	v_fmac_f32_e32 v155, v73, v125
	v_fmac_f32_e32 v156, v73, v109
	v_fmac_f32_e32 v157, v73, v97
	v_fmac_f32_e32 v154, v74, v134
	v_fmac_f32_e32 v155, v74, v118
	v_fmac_f32_e32 v156, v74, v98
	v_fmac_f32_e32 v157, v74, v86
	v_fmac_f32_e32 v154, v75, v135
	v_fmac_f32_e32 v155, v75, v119
	v_fmac_f32_e32 v156, v75, v99
	v_fmac_f32_e32 v157, v75, v87
	v_fmac_f32_e32 v154, v76, v136
	v_fmac_f32_e32 v155, v76, v120
	v_fmac_f32_e32 v156, v76, v100
	v_fmac_f32_e32 v157, v76, v88
	v_fmac_f32_e32 v154, v77, v137
	v_fmac_f32_e32 v155, v77, v121
	v_fmac_f32_e32 v156, v77, v101
	v_fmac_f32_e32 v157, v77, v89
	v_fmac_f32_e32 v154, v78, v130
	v_fmac_f32_e32 v155, v78, v114
	v_fmac_f32_e32 v156, v78, v90
	v_fmac_f32_e32 v157, v78, v82
	v_fmac_f32_e32 v154, v79, v131
	v_fmac_f32_e32 v155, v79, v115
	v_fmac_f32_e32 v156, v79, v91
	v_fmac_f32_e32 v157, v79, v83
	v_fmac_f32_e32 v154, v80, v132
	v_fmac_f32_e32 v155, v80, v116
	v_fmac_f32_e32 v156, v80, v92
	v_fmac_f32_e32 v157, v80, v84
	v_fmac_f32_e32 v154, v81, v133
	v_fmac_f32_e32 v155, v81, v117
	v_fmac_f32_e32 v156, v81, v93
	v_fmac_f32_e32 v157, v81, v85
	s_mov_b32 s0, 0
	v_add_u32_e32 v163, s0, v164
	ds_read_b128 v[2:5], v163
	ds_read_b128 v[6:9], v163 offset:32
	ds_read_b128 v[10:13], v163 offset:64
	ds_read_b128 v[14:17], v163 offset:96
	s_addk_i32 s0, 0x200
.Ltopic_loop:
	v_add_u32_e32 v163, s0, v164
	ds_read_b128 v[18:21], v163
	ds_read_b128 v[22:25], v163 offset:32
	ds_read_b128 v[26:29], v163 offset:64
	ds_read_b128 v[30:33], v163 offset:96
	s_addk_i32 s0, 0x200
	s_waitcnt lgkmcnt(4)
	v_add_f32_e32 v34, v142, v2
	v_add_f32_e32 v38, v126, v2
	v_add_f32_e32 v42, v110, v2
	v_add_f32_e32 v46, v102, v2
	v_add_f32_e32 v35, v143, v3
	v_add_f32_e32 v39, v127, v3
	v_add_f32_e32 v43, v111, v3
	v_add_f32_e32 v47, v103, v3
	v_add_f32_e32 v36, v144, v4
	v_add_f32_e32 v40, v128, v4
	v_add_f32_e32 v44, v112, v4
	v_add_f32_e32 v48, v104, v4
	v_add_f32_e32 v37, v145, v5
	v_add_f32_e32 v41, v129, v5
	v_add_f32_e32 v45, v113, v5
	v_add_f32_e32 v49, v105, v5
	v_mul_f32_e32 v162, v66, v2
	v_fma_f32 v158, v66, |v34|, v154
	v_fma_f32 v159, v66, |v38|, v155
	v_fma_f32 v160, v66, |v42|, v156
	v_fma_f32 v161, v66, |v46|, v157
	v_fmac_f32_e32 v162, v67, v3
	v_fma_f32 v158, v67, |v35|, v158
	v_fma_f32 v159, v67, |v39|, v159
	v_fma_f32 v160, v67, |v43|, v160
	v_fma_f32 v161, v67, |v47|, v161
	v_fmac_f32_e32 v162, v68, v4
	v_fma_f32 v158, v68, |v36|, v158
	v_fma_f32 v159, v68, |v40|, v159
	v_fma_f32 v160, v68, |v44|, v160
	v_fma_f32 v161, v68, |v48|, v161
	v_fmac_f32_e32 v162, v69, v5
	v_fma_f32 v158, v69, |v37|, v158
	v_fma_f32 v159, v69, |v41|, v159
	v_fma_f32 v160, v69, |v45|, v160
	v_fma_f32 v161, v69, |v49|, v161
	v_add_f32_e32 v50, v138, v6
	v_add_f32_e32 v54, v122, v6
	v_add_f32_e32 v58, v106, v6
	v_add_f32_e32 v62, v94, v6
	v_add_f32_e32 v51, v139, v7
	v_add_f32_e32 v55, v123, v7
	v_add_f32_e32 v59, v107, v7
	v_add_f32_e32 v63, v95, v7
	v_add_f32_e32 v52, v140, v8
	v_add_f32_e32 v56, v124, v8
	v_add_f32_e32 v60, v108, v8
	v_add_f32_e32 v64, v96, v8
	v_add_f32_e32 v53, v141, v9
	v_add_f32_e32 v57, v125, v9
	v_add_f32_e32 v61, v109, v9
	v_add_f32_e32 v65, v97, v9
	v_fmac_f32_e32 v162, v70, v6
	v_fma_f32 v158, v70, |v50|, v158
	v_fma_f32 v159, v70, |v54|, v159
	v_fma_f32 v160, v70, |v58|, v160
	v_fma_f32 v161, v70, |v62|, v161
	v_fmac_f32_e32 v162, v71, v7
	v_fma_f32 v158, v71, |v51|, v158
	v_fma_f32 v159, v71, |v55|, v159
	v_fma_f32 v160, v71, |v59|, v160
	v_fma_f32 v161, v71, |v63|, v161
	v_fmac_f32_e32 v162, v72, v8
	v_fma_f32 v158, v72, |v52|, v158
	v_fma_f32 v159, v72, |v56|, v159
	v_fma_f32 v160, v72, |v60|, v160
	v_fma_f32 v161, v72, |v64|, v161
	v_fmac_f32_e32 v162, v73, v9
	v_fma_f32 v158, v73, |v53|, v158
	v_fma_f32 v159, v73, |v57|, v159
	v_fma_f32 v160, v73, |v61|, v160
	v_fma_f32 v161, v73, |v65|, v161
	v_add_f32_e32 v34, v134, v10
	v_add_f32_e32 v38, v118, v10
	v_add_f32_e32 v42, v98, v10
	v_add_f32_e32 v46, v86, v10
	v_add_f32_e32 v35, v135, v11
	v_add_f32_e32 v39, v119, v11
	v_add_f32_e32 v43, v99, v11
	v_add_f32_e32 v47, v87, v11
	v_add_f32_e32 v36, v136, v12
	v_add_f32_e32 v40, v120, v12
	v_add_f32_e32 v44, v100, v12
	v_add_f32_e32 v48, v88, v12
	v_add_f32_e32 v37, v137, v13
	v_add_f32_e32 v41, v121, v13
	v_add_f32_e32 v45, v101, v13
	v_add_f32_e32 v49, v89, v13
	v_fmac_f32_e32 v162, v74, v10
	v_fma_f32 v158, v74, |v34|, v158
	v_fma_f32 v159, v74, |v38|, v159
	v_fma_f32 v160, v74, |v42|, v160
	v_fma_f32 v161, v74, |v46|, v161
	v_fmac_f32_e32 v162, v75, v11
	v_fma_f32 v158, v75, |v35|, v158
	v_fma_f32 v159, v75, |v39|, v159
	v_fma_f32 v160, v75, |v43|, v160
	v_fma_f32 v161, v75, |v47|, v161
	v_fmac_f32_e32 v162, v76, v12
	v_fma_f32 v158, v76, |v36|, v158
	v_fma_f32 v159, v76, |v40|, v159
	v_fma_f32 v160, v76, |v44|, v160
	v_fma_f32 v161, v76, |v48|, v161
	v_fmac_f32_e32 v162, v77, v13
	v_fma_f32 v158, v77, |v37|, v158
	v_fma_f32 v159, v77, |v41|, v159
	v_fma_f32 v160, v77, |v45|, v160
	v_fma_f32 v161, v77, |v49|, v161
	v_add_f32_e32 v50, v130, v14
	v_add_f32_e32 v54, v114, v14
	v_add_f32_e32 v58, v90, v14
	v_add_f32_e32 v62, v82, v14
	v_add_f32_e32 v51, v131, v15
	v_add_f32_e32 v55, v115, v15
	v_add_f32_e32 v59, v91, v15
	v_add_f32_e32 v63, v83, v15
	v_add_f32_e32 v52, v132, v16
	v_add_f32_e32 v56, v116, v16
	v_add_f32_e32 v60, v92, v16
	v_add_f32_e32 v64, v84, v16
	v_add_f32_e32 v53, v133, v17
	v_add_f32_e32 v57, v117, v17
	v_add_f32_e32 v61, v93, v17
	v_add_f32_e32 v65, v85, v17
	v_fmac_f32_e32 v162, v78, v14
	v_fma_f32 v158, v78, |v50|, v158
	v_fma_f32 v159, v78, |v54|, v159
	v_fma_f32 v160, v78, |v58|, v160
	v_fma_f32 v161, v78, |v62|, v161
	v_fmac_f32_e32 v162, v79, v15
	v_fma_f32 v158, v79, |v51|, v158
	v_fma_f32 v159, v79, |v55|, v159
	v_fma_f32 v160, v79, |v59|, v160
	v_fma_f32 v161, v79, |v63|, v161
	v_fmac_f32_e32 v162, v80, v16
	v_fma_f32 v158, v80, |v52|, v158
	v_fma_f32 v159, v80, |v56|, v159
	v_fma_f32 v160, v80, |v60|, v160
	v_fma_f32 v161, v80, |v64|, v161
	v_fmac_f32_e32 v162, v81, v17
	v_fma_f32 v158, v81, |v53|, v158
	v_fma_f32 v159, v81, |v57|, v159
	v_fma_f32 v160, v81, |v61|, v160
	v_fma_f32 v161, v81, |v65|, v161
	v_add_f32_e32 v158, v158, v162
	v_add_f32_e32 v159, v159, v162
	v_add_f32_e32 v160, v160, v162
	v_add_f32_e32 v161, v161, v162
	ds_write2_b32 v1, v158, v159 offset1:32
	ds_write2_b32 v1, v160, v161 offset0:64 offset1:96
	v_add_u32_e32 v1, 0x1000, v1
	v_add_u32_e32 v163, s0, v164
	ds_read_b128 v[2:5], v163
	ds_read_b128 v[6:9], v163 offset:32
	ds_read_b128 v[10:13], v163 offset:64
	ds_read_b128 v[14:17], v163 offset:96
	s_addk_i32 s0, 0x200
	s_waitcnt lgkmcnt(4)
	v_add_f32_e32 v34, v142, v18
	v_add_f32_e32 v38, v126, v18
	v_add_f32_e32 v42, v110, v18
	v_add_f32_e32 v46, v102, v18
	v_add_f32_e32 v35, v143, v19
	v_add_f32_e32 v39, v127, v19
	v_add_f32_e32 v43, v111, v19
	v_add_f32_e32 v47, v103, v19
	v_add_f32_e32 v36, v144, v20
	v_add_f32_e32 v40, v128, v20
	v_add_f32_e32 v44, v112, v20
	v_add_f32_e32 v48, v104, v20
	v_add_f32_e32 v37, v145, v21
	v_add_f32_e32 v41, v129, v21
	v_add_f32_e32 v45, v113, v21
	v_add_f32_e32 v49, v105, v21
	v_mul_f32_e32 v162, v66, v18
	v_fma_f32 v158, v66, |v34|, v154
	v_fma_f32 v159, v66, |v38|, v155
	v_fma_f32 v160, v66, |v42|, v156
	v_fma_f32 v161, v66, |v46|, v157
	v_fmac_f32_e32 v162, v67, v19
	v_fma_f32 v158, v67, |v35|, v158
	v_fma_f32 v159, v67, |v39|, v159
	v_fma_f32 v160, v67, |v43|, v160
	v_fma_f32 v161, v67, |v47|, v161
	v_fmac_f32_e32 v162, v68, v20
	v_fma_f32 v158, v68, |v36|, v158
	v_fma_f32 v159, v68, |v40|, v159
	v_fma_f32 v160, v68, |v44|, v160
	v_fma_f32 v161, v68, |v48|, v161
	v_fmac_f32_e32 v162, v69, v21
	v_fma_f32 v158, v69, |v37|, v158
	v_fma_f32 v159, v69, |v41|, v159
	v_fma_f32 v160, v69, |v45|, v160
	v_fma_f32 v161, v69, |v49|, v161
	v_add_f32_e32 v50, v138, v22
	v_add_f32_e32 v54, v122, v22
	v_add_f32_e32 v58, v106, v22
	v_add_f32_e32 v62, v94, v22
	v_add_f32_e32 v51, v139, v23
	v_add_f32_e32 v55, v123, v23
	v_add_f32_e32 v59, v107, v23
	v_add_f32_e32 v63, v95, v23
	v_add_f32_e32 v52, v140, v24
	v_add_f32_e32 v56, v124, v24
	v_add_f32_e32 v60, v108, v24
	v_add_f32_e32 v64, v96, v24
	v_add_f32_e32 v53, v141, v25
	v_add_f32_e32 v57, v125, v25
	v_add_f32_e32 v61, v109, v25
	v_add_f32_e32 v65, v97, v25
	v_fmac_f32_e32 v162, v70, v22
	v_fma_f32 v158, v70, |v50|, v158
	v_fma_f32 v159, v70, |v54|, v159
	v_fma_f32 v160, v70, |v58|, v160
	v_fma_f32 v161, v70, |v62|, v161
	v_fmac_f32_e32 v162, v71, v23
	v_fma_f32 v158, v71, |v51|, v158
	v_fma_f32 v159, v71, |v55|, v159
	v_fma_f32 v160, v71, |v59|, v160
	v_fma_f32 v161, v71, |v63|, v161
	v_fmac_f32_e32 v162, v72, v24
	v_fma_f32 v158, v72, |v52|, v158
	v_fma_f32 v159, v72, |v56|, v159
	v_fma_f32 v160, v72, |v60|, v160
	v_fma_f32 v161, v72, |v64|, v161
	v_fmac_f32_e32 v162, v73, v25
	v_fma_f32 v158, v73, |v53|, v158
	v_fma_f32 v159, v73, |v57|, v159
	v_fma_f32 v160, v73, |v61|, v160
	v_fma_f32 v161, v73, |v65|, v161
	v_add_f32_e32 v34, v134, v26
	v_add_f32_e32 v38, v118, v26
	v_add_f32_e32 v42, v98, v26
	v_add_f32_e32 v46, v86, v26
	v_add_f32_e32 v35, v135, v27
	v_add_f32_e32 v39, v119, v27
	v_add_f32_e32 v43, v99, v27
	v_add_f32_e32 v47, v87, v27
	v_add_f32_e32 v36, v136, v28
	v_add_f32_e32 v40, v120, v28
	v_add_f32_e32 v44, v100, v28
	v_add_f32_e32 v48, v88, v28
	v_add_f32_e32 v37, v137, v29
	v_add_f32_e32 v41, v121, v29
	v_add_f32_e32 v45, v101, v29
	v_add_f32_e32 v49, v89, v29
	v_fmac_f32_e32 v162, v74, v26
	v_fma_f32 v158, v74, |v34|, v158
	v_fma_f32 v159, v74, |v38|, v159
	v_fma_f32 v160, v74, |v42|, v160
	v_fma_f32 v161, v74, |v46|, v161
	v_fmac_f32_e32 v162, v75, v27
	v_fma_f32 v158, v75, |v35|, v158
	v_fma_f32 v159, v75, |v39|, v159
	v_fma_f32 v160, v75, |v43|, v160
	v_fma_f32 v161, v75, |v47|, v161
	v_fmac_f32_e32 v162, v76, v28
	v_fma_f32 v158, v76, |v36|, v158
	v_fma_f32 v159, v76, |v40|, v159
	v_fma_f32 v160, v76, |v44|, v160
	v_fma_f32 v161, v76, |v48|, v161
	v_fmac_f32_e32 v162, v77, v29
	v_fma_f32 v158, v77, |v37|, v158
	v_fma_f32 v159, v77, |v41|, v159
	v_fma_f32 v160, v77, |v45|, v160
	v_fma_f32 v161, v77, |v49|, v161
	v_add_f32_e32 v50, v130, v30
	v_add_f32_e32 v54, v114, v30
	v_add_f32_e32 v58, v90, v30
	v_add_f32_e32 v62, v82, v30
	v_add_f32_e32 v51, v131, v31
	v_add_f32_e32 v55, v115, v31
	v_add_f32_e32 v59, v91, v31
	v_add_f32_e32 v63, v83, v31
	v_add_f32_e32 v52, v132, v32
	v_add_f32_e32 v56, v116, v32
	v_add_f32_e32 v60, v92, v32
	v_add_f32_e32 v64, v84, v32
	v_add_f32_e32 v53, v133, v33
	v_add_f32_e32 v57, v117, v33
	v_add_f32_e32 v61, v93, v33
	v_add_f32_e32 v65, v85, v33
	v_fmac_f32_e32 v162, v78, v30
	v_fma_f32 v158, v78, |v50|, v158
	v_fma_f32 v159, v78, |v54|, v159
	v_fma_f32 v160, v78, |v58|, v160
	v_fma_f32 v161, v78, |v62|, v161
	v_fmac_f32_e32 v162, v79, v31
	v_fma_f32 v158, v79, |v51|, v158
	v_fma_f32 v159, v79, |v55|, v159
	v_fma_f32 v160, v79, |v59|, v160
	v_fma_f32 v161, v79, |v63|, v161
	v_fmac_f32_e32 v162, v80, v32
	v_fma_f32 v158, v80, |v52|, v158
	v_fma_f32 v159, v80, |v56|, v159
	v_fma_f32 v160, v80, |v60|, v160
	v_fma_f32 v161, v80, |v64|, v161
	v_fmac_f32_e32 v162, v81, v33
	v_fma_f32 v158, v81, |v53|, v158
	v_fma_f32 v159, v81, |v57|, v159
	v_fma_f32 v160, v81, |v61|, v160
	v_fma_f32 v161, v81, |v65|, v161
	v_add_f32_e32 v158, v158, v162
	v_add_f32_e32 v159, v159, v162
	v_add_f32_e32 v160, v160, v162
	v_add_f32_e32 v161, v161, v162
	ds_write2_b32 v1, v158, v159 offset1:32
	ds_write2_b32 v1, v160, v161 offset0:64 offset1:96
	v_add_u32_e32 v1, 0x1000, v1
	s_cmpk_eq_i32 s0, 0x1600
	s_cbranch_scc0 .Ltopic_loop
	v_lshl_or_b32 v1, v227, 12, v226
	s_waitcnt lgkmcnt(0)
	s_barrier
	ds_read2st64_b32 v[2:3], v1 offset0:40 offset1:42
	ds_read2st64_b32 v[4:5], v1 offset0:44 offset1:46
	ds_read2st64_b32 v[6:7], v1 offset0:48 offset1:50
	v_or_b32_e32 v13, 16, v227
	s_waitcnt lgkmcnt(2)
	v_add_f32_e32 v2, s18, v2
	v_add_f32_e32 v8, v2, v3
	ds_read2st64_b32 v[2:3], v1 offset0:52 offset1:54
	s_waitcnt lgkmcnt(2)
	v_add_f32_e32 v4, v8, v4
	v_add_f32_e32 v4, v4, v5
	s_waitcnt lgkmcnt(1)
	v_add_f32_e32 v4, v4, v6
	v_add_f32_e32 v4, v4, v7
	s_waitcnt lgkmcnt(0)
	v_add_f32_e32 v2, v4, v2
	v_add_f32_e32 v2, v2, v3
	v_mul_f32_e32 v2, 0xbfb8aa3b, v2
	v_exp_f32_e32 v2, v2
	s_nop 0
	v_add_f32_e32 v4, 1.0, v2
	v_div_scale_f32 v5, s[0:1], v4, v4, 1.0
	v_rcp_f32_e32 v6, v5
	v_div_scale_f32 v7, vcc, 1.0, v4, 1.0
	ds_read2st64_b32 v[2:3], v1 offset0:104 offset1:106
	v_fma_f32 v8, -v5, v6, 1.0
	v_fmac_f32_e32 v6, v8, v6
	v_mul_f32_e32 v8, v7, v6
	v_fma_f32 v9, -v5, v8, v7
	v_fmac_f32_e32 v8, v9, v6
	v_fma_f32 v5, -v5, v8, v7
	v_div_fmas_f32 v5, v5, v6, v8
	v_div_fixup_f32 v8, v5, v4, 1.0
	ds_read2st64_b32 v[4:5], v1 offset0:108 offset1:110
	ds_read2st64_b32 v[6:7], v1 offset0:112 offset1:114
	s_waitcnt lgkmcnt(2)
	v_add_f32_e32 v2, s18, v2
	v_add_f32_e32 v9, v2, v3
	ds_read2st64_b32 v[2:3], v1 offset0:116 offset1:118
	s_waitcnt lgkmcnt(2)
	v_add_f32_e32 v4, v9, v4
	v_add_f32_e32 v4, v4, v5
	s_waitcnt lgkmcnt(1)
	v_add_f32_e32 v4, v4, v6
	v_add_f32_e32 v4, v4, v7
	s_waitcnt lgkmcnt(0)
	v_add_f32_e32 v2, v4, v2
	v_add_f32_e32 v2, v2, v3
	v_mul_f32_e32 v2, 0xbfb8aa3b, v2
	v_exp_f32_e32 v2, v2
	v_lshlrev_b32_e32 v3, 2, v227
	v_or_b32_e32 v6, 8, v227
	v_mov_b32_e32 v7, 0x17000
	v_add_f32_e32 v10, 1.0, v2
	v_div_scale_f32 v5, s[0:1], v10, v10, 1.0
	v_rcp_f32_e32 v11, v5
	v_or_b32_e32 v4, 0x17000, v3
	v_lshl_or_b32 v12, v6, 2, v7
	v_or_b32_e32 v2, 0x17010, v3
	v_or_b32_e32 v3, 0x17030, v3
	v_lshl_or_b32 v7, v13, 2, v7
	ds_read_b32 v4, v4
	ds_read_b32 v14, v2
	ds_read_b32 v12, v12
	ds_read_b32 v15, v3
	ds_read_b32 v16, v7
	s_waitcnt lgkmcnt(4)
	v_fmaak_f32 v2, v8, v4, 0xbc23d70a
	v_max_f32_e32 v8, 0, v2
	v_fma_f32 v2, -v5, v11, 1.0
	v_fmac_f32_e32 v11, v2, v11
	v_div_scale_f32 v4, vcc, 1.0, v10, 1.0
	v_mul_f32_e32 v17, v4, v11
	v_lshl_or_b32 v18, v6, 12, v226
	ds_read2st64_b32 v[2:3], v18 offset0:40 offset1:42
	v_fma_f32 v6, -v5, v17, v4
	v_fmac_f32_e32 v17, v6, v11
	v_fma_f32 v19, -v5, v17, v4
	ds_read2st64_b32 v[4:5], v18 offset0:44 offset1:46
	ds_read2st64_b32 v[6:7], v18 offset0:48 offset1:50
	s_waitcnt lgkmcnt(2)
	v_add_f32_e32 v2, s18, v2
	v_add_f32_e32 v20, v2, v3
	ds_read2st64_b32 v[2:3], v18 offset0:52 offset1:54
	s_waitcnt lgkmcnt(2)
	v_add_f32_e32 v4, v20, v4
	v_add_f32_e32 v4, v4, v5
	s_waitcnt lgkmcnt(1)
	v_add_f32_e32 v4, v4, v6
	v_add_f32_e32 v4, v4, v7
	s_waitcnt lgkmcnt(0)
	v_add_f32_e32 v2, v4, v2
	v_add_f32_e32 v2, v2, v3
	v_mul_f32_e32 v2, 0xbfb8aa3b, v2
	v_exp_f32_e32 v2, v2
	v_div_fmas_f32 v3, v19, v11, v17
	v_div_fixup_f32 v3, v3, v10, 1.0
	v_mov_b32_e32 v9, 0xbc23d70a
	v_add_f32_e32 v10, 1.0, v2
	v_div_scale_f32 v4, s[0:1], v10, v10, 1.0
	v_rcp_f32_e32 v11, v4
	v_fmaak_f32 v2, v3, v14, 0xbc23d70a
	v_max_f32_e32 v2, 0, v2
	v_add_f32_e32 v8, v8, v2
	v_fma_f32 v2, -v4, v11, 1.0
	v_fmac_f32_e32 v11, v2, v11
	v_div_scale_f32 v5, vcc, 1.0, v10, 1.0
	v_mul_f32_e32 v14, v5, v11
	ds_read2st64_b32 v[2:3], v1 offset0:232 offset1:234
	v_fma_f32 v6, -v4, v14, v5
	v_fmac_f32_e32 v14, v6, v11
	v_fma_f32 v17, -v4, v14, v5
	ds_read2st64_b32 v[4:5], v1 offset0:236 offset1:238
	ds_read2st64_b32 v[6:7], v1 offset0:240 offset1:242
	s_waitcnt lgkmcnt(2)
	v_add_f32_e32 v2, s18, v2
	v_add_f32_e32 v18, v2, v3
	ds_read2st64_b32 v[2:3], v1 offset0:244 offset1:246
	s_waitcnt lgkmcnt(2)
	v_add_f32_e32 v1, v18, v4
	v_add_f32_e32 v1, v1, v5
	s_waitcnt lgkmcnt(1)
	v_add_f32_e32 v1, v1, v6
	v_add_f32_e32 v1, v1, v7
	s_waitcnt lgkmcnt(0)
	v_add_f32_e32 v1, v1, v2
	v_add_f32_e32 v1, v1, v3
	v_mul_f32_e32 v1, 0xbfb8aa3b, v1
	v_exp_f32_e32 v1, v1
	v_div_fmas_f32 v2, v17, v11, v14
	v_div_fixup_f32 v2, v2, v10, 1.0
	v_fmaak_f32 v2, v2, v12, 0xbc23d70a
	v_add_f32_e32 v1, 1.0, v1
	v_div_scale_f32 v4, s[0:1], v1, v1, 1.0
	v_rcp_f32_e32 v10, v4
	v_max_f32_e32 v2, 0, v2
	v_add_f32_e32 v8, v8, v2
	v_div_scale_f32 v5, vcc, 1.0, v1, 1.0
	v_fma_f32 v2, -v4, v10, 1.0
	v_fmac_f32_e32 v10, v2, v10
	v_mul_f32_e32 v11, v5, v10
	v_lshl_or_b32 v12, v13, 12, v226
	ds_read2st64_b32 v[2:3], v12 offset0:40 offset1:42
	v_fma_f32 v6, -v4, v11, v5
	v_fmac_f32_e32 v11, v6, v10
	v_fma_f32 v13, -v4, v11, v5
	ds_read2st64_b32 v[4:5], v12 offset0:44 offset1:46
	ds_read2st64_b32 v[6:7], v12 offset0:48 offset1:50
	s_waitcnt lgkmcnt(2)
	v_add_f32_e32 v2, s18, v2
	v_add_f32_e32 v14, v2, v3
	ds_read2st64_b32 v[2:3], v12 offset0:52 offset1:54
	s_waitcnt lgkmcnt(2)
	v_add_f32_e32 v4, v14, v4
	v_add_f32_e32 v4, v4, v5
	s_waitcnt lgkmcnt(1)
	v_add_f32_e32 v4, v4, v6
	v_add_f32_e32 v4, v4, v7
	s_waitcnt lgkmcnt(0)
	v_add_f32_e32 v2, v4, v2
	v_add_f32_e32 v2, v2, v3
	v_mul_f32_e32 v2, 0xbfb8aa3b, v2
	v_exp_f32_e32 v2, v2
	v_div_fmas_f32 v3, v13, v10, v11
	v_div_fixup_f32 v1, v3, v1, 1.0
	v_fmaak_f32 v1, v1, v15, 0xbc23d70a
	v_add_f32_e32 v2, 1.0, v2
	v_div_scale_f32 v3, s[0:1], v2, v2, 1.0
	v_rcp_f32_e32 v4, v3
	v_max_f32_e32 v1, 0, v1
	v_add_f32_e32 v1, v8, v1
	s_lshl_b32 s0, s42, 5
	v_fma_f32 v5, -v3, v4, 1.0
	v_fmac_f32_e32 v4, v5, v4
	v_div_scale_f32 v5, vcc, 1.0, v2, 1.0
	v_mul_f32_e32 v6, v5, v4
	v_fma_f32 v7, -v3, v6, v5
	v_fmac_f32_e32 v6, v7, v4
	v_fma_f32 v3, -v3, v6, v5
	v_div_fmas_f32 v3, v3, v4, v6
	v_div_fixup_f32 v2, v3, v2, 1.0
	v_fmac_f32_e32 v9, v2, v16
	v_max_f32_e32 v2, 0, v9
	v_add_f32_e32 v2, v1, v2
	v_mov_b32_e32 v1, 0x16800
	v_lshl_or_b32 v1, v0, 2, v1
	v_cmp_gt_u32_e32 vcc, s0, v0
	ds_write_b32 v1, v2
	s_waitcnt lgkmcnt(0)
	s_barrier
	s_and_saveexec_b64 s[0:1], vcc
	s_cbranch_execz .LBB1_57
	ds_read2st64_b32 v[2:3], v1 offset1:2
	ds_read2st64_b32 v[4:5], v1 offset0:4 offset1:6
	v_add_u32_e32 v0, s33, v0
	v_ashrrev_i32_e32 v1, 31, v0
	v_lshl_add_u64 v[6:7], v[0:1], 2, s[10:11]
	s_waitcnt lgkmcnt(1)
	v_add_f32_e32 v1, v2, v3
	s_waitcnt lgkmcnt(0)
	v_add_f32_e32 v1, v1, v4
	v_add_f32_e32 v1, v1, v5
	v_add_u32_e32 v0, 0x7d00, v0
	v_mul_f32_e32 v2, 0x3d4ccccd, v1
	v_ashrrev_i32_e32 v1, 31, v0
	v_lshl_add_u64 v[0:1], v[0:1], 2, s[10:11]
	global_store_dword v[6:7], v2, off
	global_store_dword v[0:1], v2, off
